# speedup vs baseline: 1.0964x; 1.0014x over previous
.LBB1_55:
	s_setprio 2
	v_lshrrev_b32_e32 v12, 1, v0
	v_and_b32_e32 v13, 3, v0
	v_and_or_b32 v17, v12, 12, v13
	v_and_b32_e32 v16, 16, v1
	s_lshl_b32 s7, s42, 5
	s_movk_i32 s6, 0x50
	v_or3_b32 v16, v17, v16, s7
	v_mul_lo_u32 v14, v16, s6
	v_add_u32_e32 v16, 0xf550, v14
	v_add_u32_e32 v82, v16, v116
	ds_read_b128 v[38:41], v82
	ds_read_b128 v[110:113], v82 offset:32
	s_movk_i32 s7, 0x500
	s_waitcnt vmcnt(0) lgkmcnt(1)
	v_mfma_f32_32x32x16_f16 v[18:33], v[38:41], v[2:5], 0
	v_mfma_f32_32x32x16_f16 v[2:17], v[38:41], v[6:9], 0
	s_waitcnt lgkmcnt(0)
	v_mfma_f32_32x32x16_f16 v[2:17], v[110:113], v[54:57], v[2:17]
	v_mfma_f32_32x32x16_f16 v[34:49], v[38:41], v[34:37], 0
	v_mfma_f32_32x32x16_f16 v[34:49], v[110:113], v[58:61], v[34:49]
	v_mfma_f32_32x32x16_f16 v[18:33], v[110:113], v[50:53], v[18:33]
	s_nop 5
	v_or_b32_e32 v57, 11, v71
	v_or_b32_e32 v56, 12, v71
	v_or_b32_e32 v55, 13, v71
	v_or_b32_e32 v54, 14, v71
	v_or_b32_e32 v50, 15, v71
	v_add_f32_e32 v34, v83, v34
	v_add_f32_e32 v34, v34, v75
	v_mul_f32_e32 v34, 0xbfb8aa3b, v34
	v_exp_f32_e32 v34, v34
	v_mov_b32_e32 v51, 0xf550
	v_add_f32_e32 v35, v83, v35
	v_lshl_add_u32 v51, v64, 1, v51
	v_mul_lo_u32 v52, v65, s7
	v_add_f32_e32 v35, v35, v76
	v_add_u32_e32 v80, v51, v52
	v_mul_lo_u32 v52, v70, s6
	v_add_f32_e32 v34, 1.0, v34
	v_mul_f32_e32 v35, 0xbfb8aa3b, v35
	v_add_u32_e32 v75, v51, v52
	v_add_u32_e32 v52, 0x1e0, v52
	v_rcp_f32_e32 v34, v34
	v_exp_f32_e32 v76, v35
	v_add_u32_e32 v51, v51, v52
	ds_read_u16 v52, v80
	ds_read_u16 v53, v75
	ds_read_u16 v58, v75 offset:80
	ds_read_u16 v59, v75 offset:160
	ds_read_u16 v60, v75 offset:240
	ds_read_u16 v61, v75 offset:320
	ds_read_u16 v110, v75 offset:400
	ds_read_u16 v111, v51
	s_waitcnt lgkmcnt(7)
	v_cvt_f32_f16_e32 v52, v52
	v_add_f32_e32 v18, v81, v18
	v_add_f32_e32 v36, v83, v36
	v_mul_f32_e32 v35, v72, v34
	v_mul_f32_e32 v18, v18, v34
	v_add_f32_e32 v34, 1.0, v76
	v_add_f32_e32 v36, v36, v105
	v_rcp_f32_e32 v34, v34
	v_mul_f32_e32 v36, 0xbfb8aa3b, v36
	v_mul_f32_e32 v52, v18, v52
	s_waitcnt lgkmcnt(6)
	v_cvt_f32_f16_e32 v18, v53
	v_exp_f32_e32 v36, v36
	v_add_f32_e32 v19, v81, v19
	v_mul_f32_e32 v19, v19, v34
	v_mul_f32_e32 v53, v19, v18
	v_add_f32_e32 v18, 1.0, v36
	v_rcp_f32_e32 v18, v18
	v_add_f32_e32 v36, v83, v37
	s_waitcnt lgkmcnt(5)
	v_cvt_f32_f16_e32 v19, v58
	v_add_f32_e32 v36, v36, v106
	v_mul_f32_e32 v36, 0xbfb8aa3b, v36
	v_exp_f32_e32 v36, v36
	v_add_f32_e32 v20, v81, v20
	v_fmac_f32_e32 v52, 0, v35
	v_mul_f32_e32 v72, v74, v34
	v_mul_f32_e32 v34, v77, v18
	v_mul_f32_e32 v18, v20, v18
	v_fmac_f32_e32 v53, v52, v72
	v_mul_f32_e32 v76, v35, v72
	v_mul_f32_e32 v58, v18, v19
	v_fmac_f32_e32 v58, v53, v34
	v_mul_f32_e32 v37, v76, v34
	v_add_f32_e32 v34, v83, v38
	v_add_f32_e32 v18, 1.0, v36
	v_add_f32_e32 v34, v34, v107
	v_rcp_f32_e32 v18, v18
	v_mul_f32_e32 v34, 0xbfb8aa3b, v34
	s_waitcnt lgkmcnt(4)
	v_cvt_f32_f16_e32 v19, v59
	v_exp_f32_e32 v34, v34
	v_add_f32_e32 v21, v81, v21
	v_mul_f32_e32 v20, v78, v18
	v_mul_f32_e32 v18, v21, v18
	v_add_f32_e32 v21, v83, v39
	v_mul_f32_e32 v59, v18, v19
	v_add_f32_e32 v18, 1.0, v34
	v_add_f32_e32 v21, v21, v108
	v_rcp_f32_e32 v18, v18
	v_mul_f32_e32 v21, 0xbfb8aa3b, v21
	s_waitcnt lgkmcnt(3)
	v_cvt_f32_f16_e32 v19, v60
	v_exp_f32_e32 v21, v21
	v_add_f32_e32 v22, v81, v22
	v_fmac_f32_e32 v59, v58, v20
	v_mul_f32_e32 v77, v37, v20
	v_mul_f32_e32 v20, v79, v18
	v_mul_f32_e32 v18, v22, v18
	v_mul_f32_e32 v60, v18, v19
	v_add_f32_e32 v18, 1.0, v21
	v_add_f32_e32 v21, v83, v40
	v_add_f32_e32 v21, v21, v109
	v_rcp_f32_e32 v18, v18
	v_mul_f32_e32 v21, 0xbfb8aa3b, v21
	s_waitcnt lgkmcnt(2)
	v_cvt_f32_f16_e32 v19, v61
	v_exp_f32_e32 v21, v21
	v_add_f32_e32 v22, v81, v23
	v_fmac_f32_e32 v60, v59, v20
	v_mul_f32_e32 v39, v77, v20
	v_mul_f32_e32 v20, v102, v18
	v_mul_f32_e32 v18, v22, v18
	v_mul_f32_e32 v61, v18, v19
	v_add_f32_e32 v18, 1.0, v21
	v_add_f32_e32 v21, v83, v41
	v_add_f32_e32 v21, v21, v104
	v_rcp_f32_e32 v18, v18
	v_mul_f32_e32 v21, 0xbfb8aa3b, v21
	s_waitcnt lgkmcnt(1)
	v_cvt_f32_f16_e32 v19, v110
	v_exp_f32_e32 v21, v21
	v_add_f32_e32 v22, v81, v24
	v_fmac_f32_e32 v61, v60, v20
	v_mul_f32_e32 v78, v39, v20
	v_mul_f32_e32 v20, v103, v18
	v_mul_f32_e32 v18, v22, v18
	v_mul_f32_e32 v72, v18, v19
	v_add_f32_e32 v18, 1.0, v21
	v_rcp_f32_e32 v18, v18
	v_add_f32_e32 v21, v81, v25
	v_fmac_f32_e32 v72, v61, v20
	v_mul_f32_e32 v79, v78, v20
	v_mul_f32_e32 v20, v101, v18
	v_mul_f32_e32 v18, v21, v18
	v_add_f32_e32 v21, v83, v42
	v_add_f32_e32 v21, v21, v100
	v_mul_f32_e32 v21, 0xbfb8aa3b, v21
	s_waitcnt lgkmcnt(0)
	v_cvt_f32_f16_e32 v19, v111
	v_exp_f32_e32 v21, v21
	v_add_f32_e32 v36, v83, v43
	v_mul_f32_e32 v41, v79, v20
	v_mul_f32_e32 v74, v18, v19
	v_add_f32_e32 v18, 1.0, v21
	v_fmac_f32_e32 v74, v72, v20
	v_rcp_f32_e32 v18, v18
	ds_read_u16 v19, v51 offset:80
	ds_read_u16 v20, v51 offset:160
	ds_read_u16 v21, v51 offset:240
	ds_read_u16 v22, v51 offset:320
	ds_read_u16 v23, v51 offset:400
	ds_read_u16 v24, v51 offset:480
	ds_read_u16 v25, v51 offset:560
	ds_read_u16 v42, v51 offset:640
	v_add_f32_e32 v36, v36, v98
	s_waitcnt lgkmcnt(7)
	v_cvt_f32_f16_e32 v19, v19
	v_mul_f32_e32 v36, 0xbfb8aa3b, v36
	v_exp_f32_e32 v36, v36
	v_add_f32_e32 v26, v81, v26
	v_mul_f32_e32 v34, v84, v18
	v_mul_f32_e32 v18, v26, v18
	v_mul_f32_e32 v26, v18, v19
	v_add_f32_e32 v18, 1.0, v36
	v_fmac_f32_e32 v26, v74, v34
	v_mul_f32_e32 v84, v41, v34
	v_add_f32_e32 v34, v83, v44
	v_rcp_f32_e32 v18, v18
	v_add_f32_e32 v34, v34, v97
	s_waitcnt lgkmcnt(6)
	v_cvt_f32_f16_e32 v19, v20
	v_mul_f32_e32 v34, 0xbfb8aa3b, v34
	v_exp_f32_e32 v36, v34
	v_add_f32_e32 v27, v81, v27
	v_mul_f32_e32 v20, v85, v18
	v_mul_f32_e32 v18, v27, v18
	v_mul_f32_e32 v34, v18, v19
	s_waitcnt lgkmcnt(5)
	v_cvt_f32_f16_e32 v19, v21
	v_add_f32_e32 v21, v83, v45
	v_add_f32_e32 v18, 1.0, v36
	v_add_f32_e32 v21, v21, v96
	v_rcp_f32_e32 v18, v18
	v_mul_f32_e32 v21, 0xbfb8aa3b, v21
	v_exp_f32_e32 v21, v21
	v_add_f32_e32 v27, v81, v28
	v_fmac_f32_e32 v34, v26, v20
	v_mul_f32_e32 v85, v84, v20
	v_mul_f32_e32 v20, v86, v18
	v_mul_f32_e32 v18, v27, v18
	v_mul_f32_e32 v28, v18, v19
	v_add_f32_e32 v18, 1.0, v21
	v_add_f32_e32 v21, v83, v46
	v_add_f32_e32 v21, v21, v95
	v_rcp_f32_e32 v18, v18
	v_mul_f32_e32 v21, 0xbfb8aa3b, v21
	s_waitcnt lgkmcnt(4)
	v_cvt_f32_f16_e32 v19, v22
	v_exp_f32_e32 v21, v21
	v_add_f32_e32 v22, v81, v29
	v_fmac_f32_e32 v28, v34, v20
	v_mul_f32_e32 v86, v85, v20
	v_mul_f32_e32 v20, v87, v18
	v_mul_f32_e32 v18, v22, v18
	v_mul_f32_e32 v36, v18, v19
	v_add_f32_e32 v18, 1.0, v21
	v_add_f32_e32 v21, v83, v47
	v_add_f32_e32 v21, v21, v93
	v_rcp_f32_e32 v18, v18
	v_mul_f32_e32 v21, 0xbfb8aa3b, v21
	s_waitcnt lgkmcnt(3)
	v_cvt_f32_f16_e32 v19, v23
	v_exp_f32_e32 v21, v21
	v_add_f32_e32 v22, v81, v30
	v_fmac_f32_e32 v36, v28, v20
	v_mul_f32_e32 v87, v86, v20
	v_mul_f32_e32 v20, v92, v18
	v_mul_f32_e32 v18, v22, v18
	v_mul_f32_e32 v38, v18, v19
	v_add_f32_e32 v18, 1.0, v21
	v_add_f32_e32 v21, v83, v48
	v_add_f32_e32 v21, v21, v94
	v_rcp_f32_e32 v18, v18
	v_mul_f32_e32 v21, 0xbfb8aa3b, v21
	s_waitcnt lgkmcnt(2)
	v_cvt_f32_f16_e32 v19, v24
	v_exp_f32_e32 v21, v21
	v_add_f32_e32 v22, v81, v31
	v_fmac_f32_e32 v38, v36, v20
	v_mul_f32_e32 v47, v87, v20
	v_mul_f32_e32 v20, v89, v18
	v_mul_f32_e32 v18, v22, v18
	v_mul_f32_e32 v40, v18, v19
	v_add_f32_e32 v18, 1.0, v21
	v_add_f32_e32 v21, v83, v49
	v_add_f32_e32 v21, v21, v91
	v_rcp_f32_e32 v18, v18
	v_mul_f32_e32 v21, 0xbfb8aa3b, v21
	s_waitcnt lgkmcnt(1)
	v_cvt_f32_f16_e32 v19, v25
	v_exp_f32_e32 v21, v21
	v_add_f32_e32 v22, v81, v32
	v_fmac_f32_e32 v40, v38, v20
	v_mul_f32_e32 v31, v47, v20
	v_mul_f32_e32 v20, v90, v18
	v_mul_f32_e32 v18, v22, v18
	v_mul_f32_e32 v32, v18, v19
	v_add_f32_e32 v18, 1.0, v21
	v_rcp_f32_e32 v18, v18
	s_waitcnt lgkmcnt(0)
	v_cvt_f32_f16_e32 v19, v42
	v_add_f32_e32 v21, v81, v33
	v_fmac_f32_e32 v32, v40, v20
	v_mul_f32_e32 v48, v31, v20
	v_mul_f32_e32 v20, v88, v18
	v_mul_f32_e32 v18, v21, v18
	v_mul_f32_e32 v30, v18, v19
	v_fmac_f32_e32 v30, v32, v20
	v_mul_f32_e32 v49, v48, v20
	s_and_saveexec_b64 s[6:7], s[0:1]
	s_cbranch_execz .LBB1_57
	v_add_f32_e32 v2, 0, v2
	v_add_f32_e32 v2, v2, v3
	v_add_f32_e32 v2, v2, v4
	v_add_f32_e32 v2, v2, v5
	v_add_f32_e32 v2, v2, v6
	v_add_f32_e32 v2, v2, v7
	v_add_f32_e32 v2, v2, v8
	v_add_f32_e32 v2, v2, v9
	v_add_f32_e32 v2, v2, v10
	v_add_f32_e32 v2, v2, v11
	v_add_f32_e32 v2, v2, v12
	v_add_f32_e32 v2, v2, v13
	v_add_f32_e32 v2, v2, v14
	v_mul_lo_u32 v3, v65, 21
	v_add_f32_e32 v2, v2, v15
	v_add_lshl_u32 v3, v3, v114, 2
	v_add_f32_e32 v2, v2, v16
	v_add_u32_e32 v4, 0x12450, v3
	v_add_f32_e32 v2, v2, v17
	ds_write_b32 v4, v49
	v_add_u32_e32 v4, 0x126f0, v3
	v_add_u32_e32 v3, 0x12990, v3
	ds_write_b32 v4, v30
	ds_write_b32 v3, v2
.LBB1_57:
	s_or_b64 exec, exec, s[6:7]
	s_waitcnt lgkmcnt(0)
	s_barrier
	ds_read_b128 v[6:9], v82
	ds_read_b128 v[22:25], v82 offset:32
	v_cmp_ne_u32_e32 vcc, 0, v65
	s_waitcnt lgkmcnt(1)
	v_mfma_f32_32x32x16_f16 v[2:17], v[6:9], v[118:121], 0
	s_and_saveexec_b64 s[6:7], vcc
	s_cbranch_execz .LBB1_59
	v_add_u32_e32 v27, 0x12450, v73
	v_add_u32_e32 v29, 0x126f0, v73
	ds_read_b32 v99, v29
	ds_read_b32 v27, v27
	s_waitcnt lgkmcnt(0)
	v_fmac_f32_e32 v99, 0, v27

.LBB1_66:
	s_or_b64 exec, exec, s[6:7]
	s_waitcnt lgkmcnt(6)
	v_mfma_f32_32x32x16_f16 v[2:17], v[22:25], v[122:125], v[2:17]
	s_and_saveexec_b64 s[6:7], s[0:1]
	s_cbranch_execz .LBB1_68
	s_waitcnt lgkmcnt(5)
	v_add_f32_e32 v18, 0, v29
	s_waitcnt lgkmcnt(4)
	v_add_f32_e32 v18, v18, v33
	s_waitcnt lgkmcnt(3)
	v_add_f32_e32 v18, v18, v42
	v_lshlrev_b32_e32 v67, 2, v114
	s_waitcnt lgkmcnt(2)
	v_add_f32_e32 v18, v18, v43
	v_or_b32_e32 v89, 2, v71
	v_or_b32_e32 v88, 3, v71
	v_or_b32_e32 v83, 4, v71
	v_or_b32_e32 v82, 5, v71
	v_or_b32_e32 v81, 6, v71
	v_or_b32_e32 v73, 7, v71
	v_or_b32_e32 v66, 8, v71
	v_or_b32_e32 v64, 9, v71
	v_add_f32_e32 v71, v62, v2
	v_add_u32_e32 v2, 0x12bdc, v67
	s_waitcnt lgkmcnt(1)
	v_add_f32_e32 v18, v18, v44
	ds_read_b32 v19, v27 offset:504
	ds_read_u16 v22, v80
	ds_read_u16 v23, v75
	ds_read_u16 v24, v75 offset:80
	ds_read_u16 v25, v75 offset:160
	ds_read_u16 v27, v75 offset:240
	ds_read_u16 v29, v75 offset:320
	ds_read_u16 v33, v75 offset:400
	ds_read_b32 v2, v2
	s_waitcnt lgkmcnt(9)
	v_add_f32_e32 v18, v18, v45
	v_or_b32_e32 v20, 0xb600, v67
	s_movk_i32 s0, 0x540
	s_waitcnt lgkmcnt(8)
	v_add_f32_e32 v42, v18, v19
	v_mad_u64_u32 v[18:19], s[0:1], v65, s0, v[20:21]
	s_movk_i32 s0, 0x54
	s_nop 0
	v_mad_u64_u32 v[20:21], s[8:9], v70, s0, v[20:21]
	ds_read_b32 v19, v20 offset:1176
	s_waitcnt lgkmcnt(1)
	v_add_f32_e32 v2, v42, v2
	v_fmamk_f32 v2, v2, 0x3c064b8a, v69
	v_cvt_f32_f16_e32 v69, v22
	v_max_f32_e32 v2, 0, v2
	v_mul_f32_e32 v2, 0xbfb8aa3b, v2
	v_exp_f32_e32 v2, v2
	v_mul_f32_e32 v21, 0xbfb8aa3b, v69
	v_exp_f32_e32 v22, v21
	v_cvt_f32_f16_e32 v75, v23
	v_add_f32_e32 v2, 1.0, v2
	v_rcp_f32_e32 v21, v2
	v_add_f32_e32 v2, 1.0, v22
	v_rcp_f32_e32 v80, v2
	v_mul_f32_e32 v2, 0xbfb8aa3b, v75
	v_exp_f32_e32 v2, v2
	v_cvt_f32_f16_e32 v91, v24
	v_cvt_f32_f16_e32 v94, v25
	v_cvt_f32_f16_e32 v97, v27
	v_add_f32_e32 v2, 1.0, v2
	v_rcp_f32_e32 v92, v2
	v_mul_f32_e32 v2, 0xbfb8aa3b, v91
	v_exp_f32_e32 v2, v2
	v_fmac_f32_e32 v59, v99, v77
	v_cvt_f32_f16_e32 v100, v29
	v_cvt_f32_f16_e32 v103, v33
	v_add_f32_e32 v2, 1.0, v2
	v_rcp_f32_e32 v95, v2
	v_mul_f32_e32 v2, 0xbfb8aa3b, v94
	v_exp_f32_e32 v2, v2
	ds_read2_b32 v[22:23], v20 offset1:21
	v_add_f32_e32 v90, v62, v3
	v_add_f32_e32 v93, v62, v4
	v_add_f32_e32 v2, 1.0, v2
	v_rcp_f32_e32 v77, v2
	v_mul_f32_e32 v2, 0xbfb8aa3b, v97
	v_exp_f32_e32 v2, v2
	ds_read2_b32 v[24:25], v20 offset0:42 offset1:63
	v_add_f32_e32 v96, v62, v5
	v_add_f32_e32 v98, v62, v6
	v_add_f32_e32 v2, 1.0, v2
	v_rcp_f32_e32 v101, v2
	v_mul_f32_e32 v2, 0xbfb8aa3b, v100
	v_exp_f32_e32 v2, v2
	ds_read2_b32 v[42:43], v20 offset0:84 offset1:105
	v_add_f32_e32 v102, v62, v7
	v_fmac_f32_e32 v72, v99, v79
	v_add_f32_e32 v2, 1.0, v2
	v_rcp_f32_e32 v104, v2
	v_mul_f32_e32 v2, 0xbfb8aa3b, v103
	v_exp_f32_e32 v2, v2
	ds_read_u16 v3, v51
	ds_read_u16 v4, v51 offset:80
	ds_read_u16 v5, v51 offset:160
	ds_read_u16 v6, v51 offset:240
	ds_read_u16 v7, v51 offset:320
	ds_read_u16 v33, v51 offset:400
	ds_read_u16 v79, v51 offset:480
	ds_read_u16 v106, v51 offset:560
	s_waitcnt lgkmcnt(7)
	v_cvt_f32_f16_e32 v107, v3
	s_waitcnt lgkmcnt(6)
	v_cvt_f32_f16_e32 v27, v4
	v_add_f32_e32 v2, 1.0, v2
	v_rcp_f32_e32 v108, v2
	v_mul_f32_e32 v2, 0xbfb8aa3b, v107
	v_exp_f32_e32 v2, v2
	v_fmac_f32_e32 v52, v99, v35
	s_waitcnt lgkmcnt(5)
	v_cvt_f32_f16_e32 v35, v5
	v_fmac_f32_e32 v26, v99, v84
	v_add_f32_e32 v2, 1.0, v2
	v_rcp_f32_e32 v110, v2
	v_mul_f32_e32 v2, 0xbfb8aa3b, v27
	v_exp_f32_e32 v2, v2
	s_waitcnt lgkmcnt(4)
	v_cvt_f32_f16_e32 v29, v6
	v_fmac_f32_e32 v53, v99, v76
	v_add_f32_e32 v76, v62, v11
	v_add_f32_e32 v2, 1.0, v2
	v_rcp_f32_e32 v84, v2
	v_mul_f32_e32 v2, 0xbfb8aa3b, v35
	v_exp_f32_e32 v2, v2
	v_fmac_f32_e32 v58, v99, v37
	s_waitcnt lgkmcnt(3)
	v_cvt_f32_f16_e32 v37, v7
	v_fmac_f32_e32 v60, v99, v39
	v_add_f32_e32 v2, 1.0, v2
	v_rcp_f32_e32 v11, v2
	v_mul_f32_e32 v2, 0xbfb8aa3b, v29
	v_exp_f32_e32 v2, v2
	v_fmac_f32_e32 v74, v99, v41
	s_waitcnt lgkmcnt(2)
	v_cvt_f32_f16_e32 v39, v33
	s_waitcnt lgkmcnt(1)
	v_cvt_f32_f16_e32 v41, v79
	v_add_f32_e32 v2, 1.0, v2
	v_fmac_f32_e32 v34, v99, v85
	v_rcp_f32_e32 v85, v2
	v_mul_f32_e32 v2, 0xbfb8aa3b, v37
	v_exp_f32_e32 v2, v2
	v_mul_f32_e32 v3, 0xbfb8aa3b, v39
	v_mul_f32_e32 v6, 0xbfb8aa3b, v41
	v_exp_f32_e32 v3, v3
	v_exp_f32_e32 v6, v6
	s_waitcnt lgkmcnt(0)
	v_cvt_f32_f16_e32 v33, v106
	v_add_f32_e32 v2, 1.0, v2
	v_add_f32_e32 v46, v62, v13
	v_rcp_f32_e32 v13, v2
	v_add_f32_e32 v2, 1.0, v3
	v_add_f32_e32 v6, 1.0, v6
	v_fmac_f32_e32 v28, v99, v86
	v_fmac_f32_e32 v36, v99, v87
	v_rcp_f32_e32 v86, v2
	v_add_u32_e32 v2, 0x200, v20
	v_rcp_f32_e32 v87, v6
	v_mul_f32_e32 v6, 0xbfb8aa3b, v33
	v_add_f32_e32 v105, v62, v8
	ds_read2_b32 v[44:45], v20 offset0:126 offset1:147
	v_add_f32_e32 v109, v62, v9
	v_add_f32_e32 v70, v62, v10
	ds_read2_b32 v[8:9], v20 offset0:168 offset1:189
	ds_read2_b32 v[4:5], v20 offset0:210 offset1:231
	ds_read2_b32 v[2:3], v2 offset0:124 offset1:145
	v_add_f32_e32 v10, v62, v15
	v_exp_f32_e32 v6, v6
	ds_read_b32 v15, v18
	ds_read_u16 v7, v51 offset:640
	v_mov_b32_e32 v20, v17
	v_fmac_f32_e32 v40, v99, v31
	v_add_f32_e32 v6, 1.0, v6
	v_rcp_f32_e32 v18, v6
	s_waitcnt lgkmcnt(0)
	v_cvt_f32_f16_e32 v31, v7
	v_pk_add_f32 v[6:7], v[62:63], v[20:21]
	v_fmac_f32_e32 v61, v99, v78
	v_add_f32_e32 v78, v62, v12
	v_add_f32_e32 v12, v62, v16
	v_mul_f32_e32 v16, v7, v69
	v_fmac_f32_e32 v16, v71, v52
	v_fmac_f32_e32 v15, v16, v80
	v_mul_f32_e32 v16, v7, v75
	v_fmac_f32_e32 v16, v90, v53
	v_add_f32_e32 v15, 0, v15
	v_fma_f32 v16, v16, v92, v22
	v_add_f32_e32 v15, v15, v16
	v_mul_f32_e32 v16, v7, v91
	s_movk_i32 s1, 0x7a
	v_fmac_f32_e32 v16, v93, v58
	v_fmac_f32_e32 v23, v16, v95
	v_cmp_gt_u32_e32 vcc, s1, v89
	v_mov_b32_e32 v71, v7
	v_mov_b32_e32 v79, v7
	v_cndmask_b32_e32 v16, 0, v23, vcc
	v_add_f32_e32 v15, v15, v16
	v_mul_f32_e32 v16, v7, v94
	v_fmac_f32_e32 v16, v96, v59
	v_fma_f32 v16, v16, v77, v24
	v_cmp_gt_u32_e32 vcc, s1, v88
	v_mov_b32_e32 v77, v7
	v_fmac_f32_e32 v38, v99, v47
	v_cndmask_b32_e32 v16, 0, v16, vcc
	v_add_f32_e32 v15, v15, v16
	v_mul_f32_e32 v16, v7, v97
	v_fmac_f32_e32 v16, v98, v60
	v_fmac_f32_e32 v25, v16, v101
	v_cmp_gt_u32_e32 vcc, s1, v83
	v_mov_b32_e32 v47, v7
	v_add_f32_e32 v14, v62, v14
	v_cndmask_b32_e32 v16, 0, v25, vcc
	v_add_f32_e32 v15, v15, v16
	v_mul_f32_e32 v16, v7, v100
	v_fmac_f32_e32 v16, v102, v61
	v_fma_f32 v16, v16, v104, v42
	v_cmp_gt_u32_e32 vcc, s1, v82
	v_fmac_f32_e32 v32, v99, v48
	v_fmac_f32_e32 v30, v99, v49
	v_cndmask_b32_e32 v16, 0, v16, vcc
	v_add_f32_e32 v15, v15, v16
	v_mul_f32_e32 v16, v7, v103
	v_fmac_f32_e32 v16, v105, v72
	v_fmac_f32_e32 v43, v16, v108
	v_cmp_gt_u32_e32 vcc, s1, v81
	s_nop 1
	v_cndmask_b32_e32 v16, 0, v43, vcc
	v_add_f32_e32 v15, v15, v16
	v_mul_f32_e32 v16, v7, v107
	v_fmac_f32_e32 v16, v109, v74
	v_fma_f32 v16, v16, v110, v44
	v_cmp_gt_u32_e32 vcc, s1, v73
	s_nop 1
	v_cndmask_b32_e32 v16, 0, v16, vcc
	v_add_f32_e32 v15, v15, v16
	v_pk_mul_f32 v[16:17], v[70:71], v[26:27]
	v_cmp_gt_u32_e32 vcc, s1, v66
	v_add_f32_e32 v16, v16, v17
	v_fmac_f32_e32 v45, v16, v84
	v_cndmask_b32_e32 v16, 0, v45, vcc
	v_add_f32_e32 v15, v15, v16
	v_pk_mul_f32 v[16:17], v[76:77], v[34:35]
	v_cmp_gt_u32_e32 vcc, s1, v64
	v_add_f32_e32 v16, v16, v17
	v_fma_f32 v8, v16, v11, v8
	v_pk_mul_f32 v[16:17], v[78:79], v[28:29]
	v_cndmask_b32_e32 v8, 0, v8, vcc
	v_add_f32_e32 v11, v16, v17
	v_fmac_f32_e32 v9, v11, v85
	v_cmp_gt_u32_e32 vcc, s1, v68
	v_add_f32_e32 v8, v15, v8
	v_mov_b32_e32 v15, v7
	v_cndmask_b32_e32 v9, 0, v9, vcc
	v_add_f32_e32 v11, v8, v9
	v_pk_mul_f32 v[8:9], v[46:47], v[36:37]
	v_cmp_gt_u32_e32 vcc, s1, v57
	v_add_f32_e32 v8, v8, v9
	v_fma_f32 v4, v8, v13, v4
	v_pk_mul_f32 v[8:9], v[14:15], v[38:39]
	v_cndmask_b32_e32 v4, 0, v4, vcc
	v_add_f32_e32 v8, v8, v9
	v_fmac_f32_e32 v5, v8, v86
	v_cmp_gt_u32_e32 vcc, s1, v56
	v_add_f32_e32 v4, v11, v4
	v_mov_b32_e32 v11, v7
	v_cndmask_b32_e32 v5, 0, v5, vcc
	v_add_f32_e32 v8, v4, v5
	v_pk_mul_f32 v[4:5], v[10:11], v[40:41]
	v_mov_b32_e32 v13, v7
	v_add_f32_e32 v4, v4, v5
	v_fma_f32 v2, v4, v87, v2
	v_pk_mul_f32 v[4:5], v[12:13], v[32:33]
	v_cmp_gt_u32_e32 vcc, s1, v55
	v_add_f32_e32 v4, v4, v5
	v_mul_f32_e32 v5, 0xbfb8aa3b, v31
	v_exp_f32_e32 v5, v5
	v_fmac_f32_e32 v3, v4, v18
	v_cndmask_b32_e32 v2, 0, v2, vcc
	v_cmp_gt_u32_e32 vcc, s1, v54
	v_add_f32_e32 v4, 1.0, v5
	v_rcp_f32_e32 v4, v4
	v_add_f32_e32 v2, v8, v2
	v_cndmask_b32_e32 v3, 0, v3, vcc
	v_add_f32_e32 v5, v2, v3
	v_pk_mul_f32 v[2:3], v[6:7], v[30:31]
	v_cmp_gt_u32_e32 vcc, s1, v50
	v_add_f32_e32 v2, v2, v3
	v_fmac_f32_e32 v19, v2, v4
	v_cndmask_b32_e32 v2, 0, v19, vcc
	v_mul_lo_u32 v3, v65, s0
	s_mov_b32 s0, 0x12c30
	v_add_f32_e32 v2, v5, v2
	v_add3_u32 v3, v3, v67, s0
	ds_write_b32 v3, v2
